# v15 + mLSTM gate-projection f32-MFMA loop rewritten with dwordx2 B loads, 8 loads in flight
# baseline (speedup 1.0000x reference)
; #define LAS __attribute__((address_space(3)))
; template <int NT>
; __device__ __forceinline__ void rows16_matmul(const LAS float* hfs, const float* W, int ldw, int col0, int wave, int lane, f32x4 (&acc)[NT]) {
; #pragma unroll
;     for (int jt = 0; jt < NT; ++jt) acc[jt] = (f32x4){0.f, 0.f, 0.f, 0.f};
;     const LAS float* ap = hfs + (lane & 15) * HFS_LD + wave * 256 + (lane >> 4);
;     const float* bp = W + (size_t)(wave * 256 + (lane >> 4)) * ldw + col0 + (lane & 15);
; #pragma unroll 8
;     for (int s4 = 0; s4 < 64; ++s4) {
;         const float a = ap[s4 * 4];
;         float b[NT];
; #pragma unroll
;         for (int jt = 0; jt < NT; ++jt) b[jt] = bp[(size_t)(s4 * 4) * ldw + jt * 16];
; #pragma unroll
;         for (int jt = 0; jt < NT; ++jt) acc[jt] = __builtin_amdgcn_mfma_f32_16x16x4f32(a, b[jt], acc[jt], 0, 0, 0);
;     }
; }
; __device__ __forceinline__ void ml_norm_gates_phase(LAS unsigned char* lds, int bid, int G, const float* x, const float* g, const float* sc, const float* sh,
;                                                     const float* w_in, const float* gate_b, bf16_t* hbuf, float* gates) {
;     ...
;         __syncthreads();
; #pragma unroll
;         for (int jt = 0; jt < 2; ++jt)
; #pragma unroll
;             for (int r = 0; r < 4; ++r) part[(wave * 16 + (lane >> 4) * 4 + r) * 32 + jt * 16 + (lane & 15)] = acc[jt][r];
;         __syncthreads();
;         {   const int rl = wave * 2 + (lane >> 5), col = lane & 31;
;             float sacc = gate_b[col];
; #pragma unroll
;             for (int w = 0; w < 8; ++w) sacc += part[(w * 16 + rl) * 32 + col];
;             gates[(size_t)(r0 + rl) * 32 + col] = sacc; }
.Lgt_pre:
	v_and_b32_e32 v90, 15, v0
	v_lshlrev_b32_e32 v90, 2, v90
	v_add_u32_e32 v90, 0x6000, v90
	v_mov_b32_e32 v91, 0
	v_lshl_add_u64 v[92:93], v[156:157], 0, v[90:91]
	v_mov_b32_e32 v94, v92
	v_mov_b32_e32 v95, v93
	v_mov_b32_e32 v96, 0x18200
	v_mov_b32_e32 v97, 0
	s_mov_b32 s0, 0
	global_load_dwordx2 v[20:21], v[94:95], off
	v_lshl_add_u64 v[94:95], v[94:95], 0, v[96:97]
	global_load_dwordx2 v[22:23], v[94:95], off
	v_lshl_add_u64 v[94:95], v[94:95], 0, v[96:97]
	global_load_dwordx2 v[24:25], v[94:95], off
	v_lshl_add_u64 v[94:95], v[94:95], 0, v[96:97]
	global_load_dwordx2 v[26:27], v[94:95], off
	v_lshl_add_u64 v[94:95], v[94:95], 0, v[96:97]
	global_load_dwordx2 v[28:29], v[94:95], off
	v_lshl_add_u64 v[94:95], v[94:95], 0, v[96:97]
	global_load_dwordx2 v[30:31], v[94:95], off
	v_lshl_add_u64 v[94:95], v[94:95], 0, v[96:97]
	global_load_dwordx2 v[32:33], v[94:95], off
	v_lshl_add_u64 v[94:95], v[94:95], 0, v[96:97]
	global_load_dwordx2 v[34:35], v[94:95], off
	v_lshl_add_u64 v[94:95], v[94:95], 0, v[96:97]
.Lgt_loop:
	ds_read2_b32 v[40:41], v10 offset1:4
	ds_read2_b32 v[42:43], v10 offset0:8 offset1:12
	ds_read2_b32 v[44:45], v10 offset0:16 offset1:20
	ds_read2_b32 v[46:47], v10 offset0:24 offset1:28
	v_add_u32_e32 v10, 0x80, v10
	s_add_u32 s0, s0, 1
	s_cmp_lg_u32 s0, 8
	s_cbranch_scc1 .Lgt_nl
	v_mov_b32_e32 v94, v92
	v_mov_b32_e32 v95, v93
.Lgt_nl:
	s_waitcnt vmcnt(7) lgkmcnt(3)
	v_mfma_f32_16x16x4_f32 v[6:9], v40, v20, v[6:9]
	v_mfma_f32_16x16x4_f32 v[2:5], v40, v21, v[2:5]
	global_load_dwordx2 v[20:21], v[94:95], off
	v_lshl_add_u64 v[94:95], v[94:95], 0, v[96:97]
	s_waitcnt vmcnt(7) lgkmcnt(3)
	v_mfma_f32_16x16x4_f32 v[6:9], v41, v22, v[6:9]
	v_mfma_f32_16x16x4_f32 v[2:5], v41, v23, v[2:5]
	global_load_dwordx2 v[22:23], v[94:95], off
	v_lshl_add_u64 v[94:95], v[94:95], 0, v[96:97]
	s_waitcnt vmcnt(7) lgkmcnt(2)
	v_mfma_f32_16x16x4_f32 v[6:9], v42, v24, v[6:9]
	v_mfma_f32_16x16x4_f32 v[2:5], v42, v25, v[2:5]
	global_load_dwordx2 v[24:25], v[94:95], off
	v_lshl_add_u64 v[94:95], v[94:95], 0, v[96:97]
	s_waitcnt vmcnt(7) lgkmcnt(2)
	v_mfma_f32_16x16x4_f32 v[6:9], v43, v26, v[6:9]
	v_mfma_f32_16x16x4_f32 v[2:5], v43, v27, v[2:5]
	global_load_dwordx2 v[26:27], v[94:95], off
	v_lshl_add_u64 v[94:95], v[94:95], 0, v[96:97]
	s_waitcnt vmcnt(7) lgkmcnt(1)
	v_mfma_f32_16x16x4_f32 v[6:9], v44, v28, v[6:9]
	v_mfma_f32_16x16x4_f32 v[2:5], v44, v29, v[2:5]
	global_load_dwordx2 v[28:29], v[94:95], off
	v_lshl_add_u64 v[94:95], v[94:95], 0, v[96:97]
	s_waitcnt vmcnt(7) lgkmcnt(1)
	v_mfma_f32_16x16x4_f32 v[6:9], v45, v30, v[6:9]
	v_mfma_f32_16x16x4_f32 v[2:5], v45, v31, v[2:5]
	global_load_dwordx2 v[30:31], v[94:95], off
	v_lshl_add_u64 v[94:95], v[94:95], 0, v[96:97]
	s_waitcnt vmcnt(7) lgkmcnt(0)
	v_mfma_f32_16x16x4_f32 v[6:9], v46, v32, v[6:9]
	v_mfma_f32_16x16x4_f32 v[2:5], v46, v33, v[2:5]
	global_load_dwordx2 v[32:33], v[94:95], off
	v_lshl_add_u64 v[94:95], v[94:95], 0, v[96:97]
	s_waitcnt vmcnt(7) lgkmcnt(0)
	v_mfma_f32_16x16x4_f32 v[6:9], v47, v34, v[6:9]
	v_mfma_f32_16x16x4_f32 v[2:5], v47, v35, v[2:5]
	global_load_dwordx2 v[34:35], v[94:95], off
	v_lshl_add_u64 v[94:95], v[94:95], 0, v[96:97]
	s_cbranch_scc1 .Lgt_loop
	s_waitcnt vmcnt(0)
	s_nop 7
	s_barrier
	s_nop 7
	v_and_b32_e32 v90, 15, v0
	v_lshl_add_u32 v90, v90, 2, v177
	ds_write2_b32 v90, v6, v2 offset0:0 offset1:1
	ds_write2_b32 v90, v7, v3 offset0:32 offset1:33
	ds_write2_b32 v90, v8, v4 offset0:64 offset1:65
	ds_write2_b32 v90, v9, v5 offset0:96 offset1:97
	s_waitcnt lgkmcnt(0)
	s_barrier
	global_load_dword v12, v[148:149], off
	ds_read2st64_b32 v[2:3], v175 offset1:8
	ds_read2st64_b32 v[4:5], v175 offset0:16 offset1:24
	ds_read2st64_b32 v[6:7], v175 offset0:32 offset1:40
	ds_read2st64_b32 v[8:9], v175 offset0:48 offset1:56
	v_add_u32_e32 v10, s7, v174
	v_readlane_b32 s0, v254, 44
	v_ashrrev_i32_e32 v11, 31, v10
	s_add_i32 s7, s7, s0
	v_lshlrev_b64 v[10:11], 7, v[10:11]
	v_lshl_add_u64 v[10:11], v[150:151], 0, v[10:11]
	s_cmpk_gt_i32 s7, 0x1fff
	s_waitcnt vmcnt(0) lgkmcnt(3)
	v_add_f32_e32 v2, v12, v2
	v_add_f32_e32 v2, v2, v3
	s_waitcnt lgkmcnt(2)
	v_add_f32_e32 v2, v2, v4
	v_add_f32_e32 v2, v2, v5
	s_waitcnt lgkmcnt(1)
	v_add_f32_e32 v2, v2, v6
	v_add_f32_e32 v2, v2, v7
	s_waitcnt lgkmcnt(0)
	v_add_f32_e32 v2, v2, v8
	v_add_f32_e32 v2, v2, v9
	global_store_dword v[10:11], v2, off
	s_cbranch_scc0 .LBB0_1224
